# MoE K loop heads trimmed: hoisted loop-invariant wave-uniform test (P7/P8) plus scalar-base A-staging DMA addresses (P7)
# baseline (speedup 1.0000x reference)
; #define MG_STAGE_A(b, rows, k0) do { _Pragma("unroll") for (int h_ = 0; h_ < 2; ++h_) _Pragma("unroll") for (int i_ = 0; i_ < 2; ++i_) if (rows[h_][i_] != 0xffffffffu) \
;         __builtin_amdgcn_global_load_lds((const unsigned*)((const char*)Abase + rows[h_][i_] + (k0) * 2), (PG8_LAS unsigned*)(lds + MG_SA(b, h_) + ldsw + i_ * 8192), 16, 0, 0); } while (0)
; #define MG_LDB(dst, b, h) do { _Pragma("unroll") for (int n = 0; n < 2; ++n) _Pragma("unroll") for (int k = 0; k < 2; ++k) dst[n][k] = *(const PG8_LAS bf16x8*)(lds + MG_SB(b, h) + boff + n * 2048 + k * 1024); } while (0)
; template <class Epi, bool G1> ...
;     ...
;         const bool wact = MG_WACT(cur);
;         for (int t = 0; t < NT; ++t) {
;             const bool last = (t == NT - 1), more = !last || has_next;
;             if (wact) { MG_LDB(B0, buf, 0); MG_LDB(B1, buf, 1); }
;             if (!last) { MG_STAGE_A(buf ^ 1, rowC, (t + 1) * BK); }
.LBB0_1075:
	s_mov_b32 s70, s46
	s_add_u32 s74, s44, 0x70000080
	s_addc_u32 s75, s45, 0
	s_andn2_b64 vcc, exec, s[36:37]
	s_lshl_b32 s71, s46, 15
	s_cbranch_vccz .LBB0_1082
	s_xor_b32 s72, s71, 0x8000
	s_and_saveexec_b64 s[46:47], s[14:15]
	s_cbranch_execnz .LBB0_1083
